# v048 + P13 first-half row sums moved from the tile tail into the wait for the second QK MFMA results (MFMA-shadow fill)
# baseline (speedup 1.0000x reference)
.LBB0_2751:
	v_add_u32_e32 v179, s39, v151
	v_add_u32_e32 v225, v179, v155
	v_add_u32_e32 v224, v179, v181
	v_add_u32_e32 v223, v179, v219
	s_waitcnt lgkmcnt(0)
	v_lshrrev_b32_e32 v82, v163, v226
	v_bfe_i32 v83, v82, 26, 1
	v_bitop3_b32 v96, v16, s28, v83 bitop3:0xe4
	v_bfe_i32 v83, v82, 25, 1
	v_bitop3_b32 v95, v13, s28, v83 bitop3:0xe4
	v_bfe_i32 v83, v82, 24, 1
	v_bitop3_b32 v94, v14, s28, v83 bitop3:0xe4
	v_bfe_i32 v83, v82, 19, 1
	v_bitop3_b32 v93, v11, s28, v83 bitop3:0xe4
	v_bfe_i32 v83, v82, 18, 1
	v_bitop3_b32 v92, v12, s28, v83 bitop3:0xe4
	v_bfe_i32 v83, v82, 17, 1
	v_add_u32_e32 v226, v179, v153
	v_bitop3_b32 v91, v9, s28, v83 bitop3:0xe4
	v_bfe_i32 v83, v82, 16, 1
	ds_read_b128 v[186:189], v226
	v_bitop3_b32 v90, v10, s28, v83 bitop3:0xe4
	v_bfe_i32 v83, v82, 11, 1
	v_bitop3_b32 v89, v7, s28, v83 bitop3:0xe4
	v_bfe_i32 v83, v82, 10, 1
	v_bitop3_b32 v88, v8, s28, v83 bitop3:0xe4
	v_bfe_i32 v83, v82, 9, 1
	v_bitop3_b32 v87, v5, s28, v83 bitop3:0xe4
	v_bfe_i32 v83, v82, 8, 1
	v_bitop3_b32 v86, v6, s28, v83 bitop3:0xe4
	v_bfe_i32 v83, v82, 3, 1
	v_bfe_i32 v84, v82, 27, 1
	v_bitop3_b32 v85, v3, s28, v83 bitop3:0xe4
	v_bfe_i32 v83, v82, 2, 1
	v_bitop3_b32 v97, v15, s28, v84 bitop3:0xe4
	v_bitop3_b32 v84, v4, s28, v83 bitop3:0xe4
	v_bfe_i32 v83, v82, 1, 1
	v_bfe_i32 v82, v82, 0, 1
	v_bitop3_b32 v83, v1, s28, v83 bitop3:0xe4
	v_bitop3_b32 v82, v2, s28, v82 bitop3:0xe4
	v_add_u32_e32 v179, s39, v17
	s_add_i32 s14, s37, 1
	s_waitcnt lgkmcnt(0)
	v_mfma_f32_32x32x16_bf16 v[98:113], v[186:189], v[114:117], v[82:97]
	s_cmp_lg_u32 s37, 2
	s_cselect_b32 s37, s14, 0
	s_add_u32 s0, s0, 0x4000
	s_addc_u32 s1, s1, 0
	s_add_i32 s38, s38, 1
	s_cmp_eq_u32 s36, s0
	v_add_u32_e32 v146, 8, v146
	v_mfma_f32_32x32x16_bf16 v[82:97], v[186:189], v[130:133], v[82:97]
	ds_read_b128 v[186:189], v225
	s_waitcnt lgkmcnt(0)
	v_mfma_f32_32x32x16_bf16 v[98:113], v[186:189], v[118:121], v[98:113]
	v_mfma_f32_32x32x16_bf16 v[82:97], v[186:189], v[134:137], v[82:97]
	ds_read_b128 v[186:189], v224
	s_waitcnt lgkmcnt(0)
	v_mfma_f32_32x32x16_bf16 v[98:113], v[186:189], v[122:125], v[98:113]
	v_mfma_f32_32x32x16_bf16 v[82:97], v[186:189], v[138:141], v[82:97]
	ds_read_b128 v[186:189], v223
	s_waitcnt lgkmcnt(0)
	v_mfma_f32_32x32x16_bf16 v[98:113], v[186:189], v[126:129], v[98:113]
	v_mfma_f32_32x32x16_bf16 v[82:97], v[186:189], v[142:145], v[82:97]
	s_nop 10
	v_exp_f32_e32 v190, v98
	v_exp_f32_e32 v191, v99
	v_exp_f32_e32 v192, v100
	v_exp_f32_e32 v193, v101
	s_nop 0
	ds_read_b64_tr_b16 v[98:99], v179 offset:49152
	ds_read_b64_tr_b16 v[100:101], v179 offset:50176
	v_exp_f32_e32 v188, v102
	v_exp_f32_e32 v189, v103
	v_exp_f32_e32 v186, v104
	v_exp_f32_e32 v187, v105
	ds_read_b64_tr_b16 v[212:213], v179 offset:50688
	ds_read_b64_tr_b16 v[210:211], v179 offset:49664
	v_exp_f32_e32 v204, v82
	v_exp_f32_e32 v205, v83
	v_exp_f32_e32 v208, v84
	v_exp_f32_e32 v209, v85
	v_exp_f32_e32 v200, v86
	v_exp_f32_e32 v201, v87
	v_exp_f32_e32 v196, v88
	v_exp_f32_e32 v197, v89
	v_cvt_pk_bf16_f32 v102, v190, v191
	v_cvt_pk_bf16_f32 v103, v192, v193
	v_cvt_pk_bf16_f32 v104, v188, v189
	v_cvt_pk_bf16_f32 v105, v186, v187
	v_cvt_pk_bf16_f32 v82, v204, v205
	v_cvt_pk_bf16_f32 v83, v208, v209
	s_waitcnt lgkmcnt(2)
	v_mfma_f32_32x32x16_bf16 v[66:81], v[98:101], v[102:105], v[66:81]
	v_cvt_pk_bf16_f32 v84, v200, v201
	v_cvt_pk_bf16_f32 v85, v196, v197
	v_exp_f32_e32 v206, v106
	v_exp_f32_e32 v207, v107
	v_exp_f32_e32 v202, v108
	v_exp_f32_e32 v203, v109
	v_exp_f32_e32 v198, v110
	s_waitcnt lgkmcnt(0)
	v_mfma_f32_32x32x16_bf16 v[50:65], v[210:213], v[102:105], v[50:65]
	v_exp_f32_e32 v199, v111
	v_exp_f32_e32 v194, v112
	v_exp_f32_e32 v195, v113
	v_exp_f32_e32 v216, v90
	v_exp_f32_e32 v217, v91
	v_exp_f32_e32 v214, v92
	v_exp_f32_e32 v215, v93
	v_mfma_f32_32x32x16_bf16 v[34:49], v[98:101], v[82:85], v[34:49]
	v_cvt_pk_bf16_f32 v86, v206, v207
	v_cvt_pk_bf16_f32 v87, v202, v203
	v_cvt_pk_bf16_f32 v88, v198, v199
	v_cvt_pk_bf16_f32 v89, v194, v195
	v_mfma_f32_32x32x16_bf16 v[18:33], v[210:213], v[82:85], v[18:33]
	ds_read_b64_tr_b16 v[82:83], v179 offset:51200
	ds_read_b64_tr_b16 v[84:85], v179 offset:52224
	ds_read_b64_tr_b16 v[100:101], v179 offset:52736
	ds_read_b64_tr_b16 v[98:99], v179 offset:51712
	v_exp_f32_e32 v212, v94
	v_exp_f32_e32 v213, v95
	v_exp_f32_e32 v210, v96
	v_exp_f32_e32 v211, v97
	s_waitcnt lgkmcnt(2)
	v_mfma_f32_32x32x16_bf16 v[66:81], v[82:85], v[86:89], v[66:81]
	s_waitcnt lgkmcnt(0)
	v_mfma_f32_32x32x16_bf16 v[50:65], v[98:101], v[86:89], v[50:65]
	v_cvt_pk_bf16_f32 v86, v216, v217
	v_cvt_pk_bf16_f32 v87, v214, v215
	v_cvt_pk_bf16_f32 v88, v212, v213
	v_cvt_pk_bf16_f32 v89, v210, v211
	s_nop 1
	v_mfma_f32_32x32x16_bf16 v[34:49], v[82:85], v[86:89], v[34:49]
	v_lshrrev_b32_e32 v82, v163, v227
	v_bfe_i32 v83, v82, 26, 1
	v_bitop3_b32 v96, v16, s28, v83 bitop3:0xe4
	v_bfe_i32 v83, v82, 25, 1
	v_bitop3_b32 v95, v13, s28, v83 bitop3:0xe4
	v_bfe_i32 v83, v82, 24, 1
	v_bitop3_b32 v94, v14, s28, v83 bitop3:0xe4
	v_bfe_i32 v83, v82, 19, 1
	v_bitop3_b32 v93, v11, s28, v83 bitop3:0xe4
	v_bfe_i32 v83, v82, 18, 1
	v_bitop3_b32 v92, v12, s28, v83 bitop3:0xe4
	v_bfe_i32 v83, v82, 17, 1
	v_bitop3_b32 v91, v9, s28, v83 bitop3:0xe4
	v_bfe_i32 v83, v82, 16, 1
	ds_read_b128 v[226:229], v226 offset:4096
	v_bitop3_b32 v90, v10, s28, v83 bitop3:0xe4
	v_bfe_i32 v83, v82, 11, 1
	v_mfma_f32_32x32x16_bf16 v[18:33], v[98:101], v[86:89], v[18:33]
	v_bitop3_b32 v89, v7, s28, v83 bitop3:0xe4
	v_bfe_i32 v83, v82, 10, 1
	v_bitop3_b32 v88, v8, s28, v83 bitop3:0xe4
	v_bfe_i32 v83, v82, 9, 1
	v_bitop3_b32 v87, v5, s28, v83 bitop3:0xe4
	v_bfe_i32 v83, v82, 8, 1
	v_bitop3_b32 v86, v6, s28, v83 bitop3:0xe4
	v_bfe_i32 v83, v82, 3, 1
	v_bfe_i32 v84, v82, 27, 1
	v_bitop3_b32 v85, v3, s28, v83 bitop3:0xe4
	v_bfe_i32 v83, v82, 2, 1
	v_bitop3_b32 v97, v15, s28, v84 bitop3:0xe4
	v_bitop3_b32 v84, v4, s28, v83 bitop3:0xe4
	v_bfe_i32 v83, v82, 1, 1
	v_bfe_i32 v82, v82, 0, 1
	v_bitop3_b32 v83, v1, s28, v83 bitop3:0xe4
	v_bitop3_b32 v82, v2, s28, v82 bitop3:0xe4
	s_waitcnt lgkmcnt(0)
	s_nop 0
	v_mfma_f32_32x32x16_bf16 v[98:113], v[226:229], v[114:117], v[82:97]
	v_mfma_f32_32x32x16_bf16 v[82:97], v[226:229], v[130:133], v[82:97]
	ds_read_b128 v[226:229], v225 offset:4096
	s_waitcnt lgkmcnt(0)
	v_mfma_f32_32x32x16_bf16 v[98:113], v[226:229], v[118:121], v[98:113]
	v_mfma_f32_32x32x16_bf16 v[82:97], v[226:229], v[134:137], v[82:97]
	ds_read_b128 v[224:227], v224 offset:4096
	s_waitcnt lgkmcnt(0)
	v_mfma_f32_32x32x16_bf16 v[98:113], v[224:227], v[122:125], v[98:113]
	v_mfma_f32_32x32x16_bf16 v[82:97], v[224:227], v[138:141], v[82:97]
	ds_read_b128 v[224:227], v223 offset:4096
	s_waitcnt lgkmcnt(0)
	v_mfma_f32_32x32x16_bf16 v[98:113], v[224:227], v[126:129], v[98:113]
	v_mfma_f32_32x32x16_bf16 v[82:97], v[224:227], v[142:145], v[82:97]
	v_add_f32_e64 v240, v190, 0
	v_add_f32_e64 v242, v204, 0
	v_add_f32_e64 v241, v191, 0
	v_add_f32_e64 v243, v205, 0
	v_add_f32_e64 v240, v192, v240
	v_add_f32_e64 v242, v208, v242
	v_add_f32_e64 v241, v193, v241
	v_add_f32_e64 v243, v209, v243
	v_pk_add_f32 v[240:241], v[188:189], v[240:241]
	v_pk_add_f32 v[242:243], v[200:201], v[242:243]
	v_pk_add_f32 v[240:241], v[186:187], v[240:241]
	v_pk_add_f32 v[242:243], v[196:197], v[242:243]
	v_pk_add_f32 v[240:241], v[206:207], v[240:241]
	v_pk_add_f32 v[242:243], v[216:217], v[242:243]
	v_pk_add_f32 v[240:241], v[202:203], v[240:241]
	v_pk_add_f32 v[242:243], v[214:215], v[242:243]
	v_pk_add_f32 v[240:241], v[198:199], v[240:241]
	v_pk_add_f32 v[242:243], v[212:213], v[242:243]
	v_pk_add_f32 v[240:241], v[194:195], v[240:241]
	v_pk_add_f32 v[242:243], v[210:211], v[242:243]
	v_exp_f32_e32 v228, v98
	v_exp_f32_e32 v229, v99
	v_exp_f32_e32 v230, v100
	v_exp_f32_e32 v231, v101
	ds_read_b64_tr_b16 v[98:99], v179 offset:53248
	ds_read_b64_tr_b16 v[100:101], v179 offset:54272
	v_exp_f32_e32 v232, v102
	v_exp_f32_e32 v233, v103
	v_exp_f32_e32 v234, v104
	v_exp_f32_e32 v235, v105
	ds_read_b64_tr_b16 v[226:227], v179 offset:54784
	ds_read_b64_tr_b16 v[224:225], v179 offset:53760
	v_cvt_pk_bf16_f32 v102, v228, v229
	v_cvt_pk_bf16_f32 v103, v230, v231
	v_cvt_pk_bf16_f32 v104, v232, v233
	v_cvt_pk_bf16_f32 v105, v234, v235
	v_exp_f32_e32 v236, v86
	v_exp_f32_e32 v237, v87
	s_waitcnt lgkmcnt(2)
	v_mfma_f32_32x32x16_bf16 v[66:81], v[98:101], v[102:105], v[66:81]
	v_exp_f32_e32 v238, v88
	v_exp_f32_e32 v239, v89
	v_exp_f32_e32 v106, v106
	v_exp_f32_e32 v107, v107
	v_exp_f32_e32 v108, v108
	v_exp_f32_e32 v109, v109
	v_exp_f32_e32 v110, v110
	s_waitcnt lgkmcnt(0)
	v_mfma_f32_32x32x16_bf16 v[50:65], v[224:227], v[102:105], v[50:65]
	v_exp_f32_e32 v102, v82
	v_exp_f32_e32 v103, v83
	v_exp_f32_e32 v104, v84
	v_exp_f32_e32 v105, v85
	v_cvt_pk_bf16_f32 v84, v236, v237
	v_cvt_pk_bf16_f32 v82, v102, v103
	v_cvt_pk_bf16_f32 v85, v238, v239
	v_cvt_pk_bf16_f32 v83, v104, v105
	v_exp_f32_e32 v111, v111
	v_exp_f32_e32 v112, v112
	v_mfma_f32_32x32x16_bf16 v[34:49], v[98:101], v[82:85], v[34:49]
	v_exp_f32_e32 v113, v113
	v_exp_f32_e32 v90, v90
	v_exp_f32_e32 v91, v91
	v_exp_f32_e32 v92, v92
	v_exp_f32_e32 v93, v93
	v_exp_f32_e32 v94, v94
	v_exp_f32_e32 v95, v95
	v_mfma_f32_32x32x16_bf16 v[18:33], v[224:227], v[82:85], v[18:33]
	ds_read_b64_tr_b16 v[82:83], v179 offset:55296
	ds_read_b64_tr_b16 v[84:85], v179 offset:56320
	ds_read_b64_tr_b16 v[100:101], v179 offset:56832
	ds_read_b64_tr_b16 v[98:99], v179 offset:55808
	v_exp_f32_e32 v96, v96
	v_exp_f32_e32 v97, v97
	v_cvt_pk_bf16_f32 v86, v106, v107
	v_cvt_pk_bf16_f32 v87, v108, v109
	v_cvt_pk_bf16_f32 v88, v110, v111
	v_cvt_pk_bf16_f32 v89, v112, v113
	s_waitcnt lgkmcnt(2)
	s_nop 0
	v_mfma_f32_32x32x16_bf16 v[66:81], v[82:85], v[86:89], v[66:81]
	s_waitcnt lgkmcnt(0)
	v_mfma_f32_32x32x16_bf16 v[50:65], v[98:101], v[86:89], v[50:65]
	v_cvt_pk_bf16_f32 v86, v90, v91
	v_cvt_pk_bf16_f32 v87, v92, v93
	v_cvt_pk_bf16_f32 v88, v94, v95
	v_cvt_pk_bf16_f32 v89, v96, v97
	s_nop 1
	v_mfma_f32_32x32x16_bf16 v[34:49], v[82:85], v[86:89], v[34:49]
	v_add_f32_e64 v84, v228, 0
	v_add_f32_e64 v85, v229, 0
	v_pk_add_f32 v[84:85], v[230:231], v[84:85]
	v_pk_add_f32 v[84:85], v[232:233], v[84:85]
	v_mfma_f32_32x32x16_bf16 v[18:33], v[98:101], v[86:89], v[18:33]
	v_add_f32_e64 v88, v102, 0
	v_add_f32_e64 v89, v103, 0
	v_pk_add_f32 v[88:89], v[104:105], v[88:89]
	v_pk_add_f32 v[88:89], v[236:237], v[88:89]
	v_pk_add_f32 v[84:85], v[234:235], v[84:85]
	v_pk_add_f32 v[88:89], v[238:239], v[88:89]
	v_pk_add_f32 v[84:85], v[106:107], v[84:85]
	v_pk_add_f32 v[88:89], v[90:91], v[88:89]
	v_pk_add_f32 v[84:85], v[108:109], v[84:85]
	v_pk_add_f32 v[88:89], v[92:93], v[88:89]
	v_pk_add_f32 v[84:85], v[110:111], v[84:85]
	v_pk_add_f32 v[88:89], v[94:95], v[88:89]
	v_pk_add_f32 v[84:85], v[112:113], v[84:85]
	v_pk_add_f32 v[88:89], v[96:97], v[88:89]
	v_pk_add_f32 v[82:83], v[240:241], v[84:85]
	v_pk_add_f32 v[84:85], v[242:243], v[88:89]
	v_mov_b32_e32 v86, v82
	v_mov_b32_e32 v87, v84
	v_mov_b32_e32 v84, v83
	v_pk_add_f32 v[82:83], v[86:87], v[84:85]
	s_nop 0
	v_pk_add_f32 v[184:185], v[184:185], v[82:83]
	s_cbranch_scc1 .LBB0_2745
